# speedup vs baseline: 1.0203x; 1.0094x over previous
.LBB0_24:
	s_lshl_b32 s10, s14, 4
	s_lshl_b32 s11, s14, 6
	v_cndmask_b32_e64 v71, 0, 1, s[8:9]
	s_or_b32 s20, s10, 1
	v_or_b32_e32 v73, s11, v36
	v_cmp_ne_u32_e32 vcc, 1, v71
	v_readlane_b32 s28, v4, s10
	v_or_b32_e32 v71, s11, v21
	v_or_b32_e32 v74, s11, v37
	v_readlane_b32 s31, v4, s20
	ds_bpermute_b32 v84, v73, v2
	v_bitop3_b32 v72, s11, 12, v21 bitop3:0x36
	v_or_b32_e32 v75, s11, v38
	v_or_b32_e32 v76, s11, v39
	ds_bpermute_b32 v78, v71, v2 offset:8
	ds_bpermute_b32 v79, v71, v3 offset:8
	ds_bpermute_b32 v80, v71, v4 offset:8
	ds_bpermute_b32 v85, v73, v3
	ds_bpermute_b32 v87, v74, v2
	ds_bpermute_b32 v88, v74, v3
	v_mov_b32_e32 v71, s28
	v_fma_f32 v98, v71, v67, v70
	v_fma_f32 v99, -v71, v68, v69
	v_fma_f32 v100, v71, v65, v64
	v_fma_f32 v101, -v71, v66, v55
	v_mov_b32_e32 v102, s31
	v_fma_f32 v68, v71, v69, v68
	v_fma_f32 v67, -v71, v70, v67
	v_fma_f32 v55, v71, v55, v66
	v_fma_f32 v64, -v71, v64, v65
	v_fma_f32 v107, v102, v60, v63
	v_fma_f32 v109, v102, v56, v59
	v_fma_f32 v110, -v102, v57, v58
	v_fma_f32 v60, -v102, v63, v60
	v_fma_f32 v57, v102, v58, v57
	v_fma_f32 v56, -v102, v59, v56
	ds_bpermute_b32 v58, v19, v67
	ds_bpermute_b32 v59, v19, v68
	ds_bpermute_b32 v63, v19, v55
	s_waitcnt lgkmcnt(4)
	v_mul_f32 v122, v84, v87
	s_waitcnt lgkmcnt(3)
	v_mul_f32 v84, v84, v88
	s_or_b32 s21, s10, 8
	s_or_b32 s15, s10, 9
	v_readlane_b32 s27, v3, s10
	v_or_b32_e32 v77, s11, v40
	ds_bpermute_b32 v81, v72, v2
	ds_bpermute_b32 v83, v72, v4
	ds_bpermute_b32 v92, v75, v2
	ds_bpermute_b32 v93, v75, v3
	ds_bpermute_b32 v94, v76, v2
	ds_bpermute_b32 v95, v76, v3
	v_fma_f32 v108, -v102, v61, v62
	v_fma_f32 v61, v102, v62, v61
	ds_bpermute_b32 v62, v19, v64
	s_waitcnt lgkmcnt(2)
	v_mul_f32 v123, v92, v94
	v_fma_f32 v88, -v85, v88, v122
	v_fma_f32 v84, v85, v87, v84
	v_fma_f32 v63, -v83, v63, v67
	v_fma_f32 v55, v80, v58, v55
	v_fma_f32 v58, -v80, v59, v64
	s_waitcnt lgkmcnt(1)
	v_fma_f32 v85, -v93, v95, v123
	v_mul_f32 v59, v88, v78
	v_mul_f32 v64, v88, v79
	v_mul_f32 v67, v88, v81
	v_readlane_b32 s19, v2, s10
	v_readlane_b32 s29, v2, s20
	v_readlane_b32 s30, v3, s20
	ds_bpermute_b32 v82, v72, v3
	v_mov_b32_e32 v91, s27
	v_readlane_b32 s27, v2, s21
	v_readlane_b32 s28, v2, s15
	v_readlane_b32 s33, v3, s21
	v_readlane_b32 s34, v3, s15
	ds_bpermute_b32 v96, v77, v2
	ds_bpermute_b32 v97, v77, v3
	ds_bpermute_b32 v112, v19, v101
	ds_bpermute_b32 v113, v19, v100
	ds_bpermute_b32 v114, v19, v60
	ds_bpermute_b32 v115, v19, v61
	ds_bpermute_b32 v116, v19, v56
	ds_bpermute_b32 v117, v19, v57
	ds_bpermute_b32 v118, v19, v108
	ds_bpermute_b32 v119, v19, v107
	ds_bpermute_b32 v120, v19, v110
	v_mul_f32 v92, v92, v95
	s_waitcnt lgkmcnt(12)
	v_fma_f32 v62, v83, v62, v68
	s_waitcnt lgkmcnt(11)
	v_mul_f32 v68, v88, v82
	s_waitcnt lgkmcnt(10)
	v_mul_f32 v88, v85, v96
	s_waitcnt lgkmcnt(9)
	v_mul_f32 v85, v85, v97
	v_fma_f32 v59, -v84, v79, v59
	v_fma_f32 v87, v93, v94, v92
	v_fma_f32 v64, v84, v78, v64
	v_fma_f32 v67, -v84, v82, v67
	ds_bpermute_b32 v86, v73, v4
	v_fma_f32 v78, -v87, v97, v88
	v_mov_b32_e32 v90, s19
	v_mov_b32_e32 v65, s29
	v_mov_b32_e32 v66, s30
	v_mov_b32_e32 v103, s27
	v_mov_b32_e32 v104, s33
	v_mov_b32_e32 v105, s28
	v_mov_b32_e32 v106, s34
	ds_bpermute_b32 v102, v19, v99
	ds_bpermute_b32 v111, v19, v98
	ds_bpermute_b32 v121, v19, v109
	s_waitcnt lgkmcnt(12)
	v_fma_f32 v92, v83, v112, v98
	s_waitcnt lgkmcnt(11)
	v_fma_f32 v93, -v83, v113, v99
	s_waitcnt lgkmcnt(2)
	v_fma_f32 v94, v80, v102, v100
	s_waitcnt lgkmcnt(1)
	v_fma_f32 v95, -v80, v111, v101
	v_fma_f32 v98, v83, v120, v107
	s_waitcnt lgkmcnt(0)
	v_fma_f32 v99, -v83, v121, v108
	v_fma_f32 v100, v80, v118, v109
	v_fma_f32 v101, -v80, v119, v110
	v_fma_f32 v61, v83, v116, v61
	v_fma_f32 v60, -v83, v117, v60
	v_fma_f32 v57, v80, v114, v57
	v_fma_f32 v56, -v80, v115, v56
	ds_swizzle_b32 v80, v58 offset:swizzle(BITMASK_PERM,"iippp")
	ds_swizzle_b32 v83, v55 offset:swizzle(BITMASK_PERM,"iippp")
	v_fma_f32 v68, v84, v81, v68
	v_fma_f32 v79, v87, v96, v85
	ds_swizzle_b32 v81, v56 offset:swizzle(BITMASK_PERM,"iippp")
	ds_swizzle_b32 v82, v57 offset:swizzle(BITMASK_PERM,"iippp")
	ds_swizzle_b32 v84, v60 offset:swizzle(BITMASK_PERM,"iippp")
	ds_swizzle_b32 v85, v61 offset:swizzle(BITMASK_PERM,"iippp")
	ds_swizzle_b32 v87, v101 offset:swizzle(BITMASK_PERM,"iippp")
	ds_swizzle_b32 v88, v100 offset:swizzle(BITMASK_PERM,"iippp")
	v_mul_f32 v112, v59, v90
	v_mul_f32 v113, v59, v91
	v_mul_f32 v114, v59, v65
	v_mul_f32 v59, v59, v66
	v_mul_f32 v115, v67, v90
	v_mul_f32 v116, v67, v91
	v_mul_f32 v117, v67, v65
	v_mul_f32 v67, v67, v66
	v_mul_f32 v118, v78, v103
	v_mul_f32 v119, v78, v104
	v_mul_f32 v120, v78, v105
	v_mul_f32 v78, v78, v106
	ds_swizzle_b32 v102, v63 offset:swizzle(BITMASK_PERM,"iippp")
	ds_swizzle_b32 v107, v62 offset:swizzle(BITMASK_PERM,"iippp")
	ds_swizzle_b32 v108, v95 offset:swizzle(BITMASK_PERM,"iippp")
	ds_swizzle_b32 v109, v94 offset:swizzle(BITMASK_PERM,"iippp")
	ds_swizzle_b32 v110, v93 offset:swizzle(BITMASK_PERM,"iippp")
	ds_swizzle_b32 v111, v92 offset:swizzle(BITMASK_PERM,"iippp")
	ds_swizzle_b32 v96, v99 offset:swizzle(BITMASK_PERM,"iippp")
	ds_swizzle_b32 v97, v98 offset:swizzle(BITMASK_PERM,"iippp")
	v_fma_f32 v112, -v64, v91, v112
	v_fma_f32 v113, v64, v90, v113
	v_fma_f32 v114, -v64, v66, v114
	v_fma_f32 v59, v64, v65, v59
	v_fma_f32 v64, -v68, v91, v115
	v_fma_f32 v90, v68, v90, v116
	v_fma_f32 v66, -v68, v66, v117
	v_fma_f32 v65, v68, v65, v67
	v_fma_f32 v67, -v79, v104, v118
	v_fma_f32 v68, v79, v103, v119
	v_fma_f32 v91, -v79, v106, v120
	v_fma_f32 v78, v79, v105, v78
	s_waitcnt lgkmcnt(3)
	v_fma_f32 v79, v86, v110, v92
	s_waitcnt lgkmcnt(2)
	v_fma_f32 v92, -v86, v111, v93
	v_fma_f32 v93, v86, v108, v94
	v_fma_f32 v94, -v86, v109, v95
	v_fma_f32 v62, v86, v102, v62
	v_fma_f32 v63, -v86, v107, v63
	v_fma_f32 v55, v86, v80, v55
	v_fma_f32 v58, -v86, v83, v58
	s_waitcnt lgkmcnt(1)
	v_fma_f32 v80, v86, v96, v98
	s_waitcnt lgkmcnt(0)
	v_fma_f32 v83, -v86, v97, v99
	v_fma_f32 v87, v86, v87, v100
	v_fma_f32 v88, -v86, v88, v101
	v_fma_f32 v61, v86, v84, v61
	v_fma_f32 v60, -v86, v85, v60
	v_fma_f32 v57, v86, v81, v57
	v_fma_f32 v56, -v86, v82, v56
	ds_swizzle_b32 v81, v58 offset:swizzle(BITMASK_PERM,"ppiip")
	ds_swizzle_b32 v82, v55 offset:swizzle(BITMASK_PERM,"ppiip")
	ds_swizzle_b32 v84, v63 offset:swizzle(BITMASK_PERM,"ppiip")
	ds_swizzle_b32 v85, v62 offset:swizzle(BITMASK_PERM,"ppiip")
	ds_swizzle_b32 v86, v94 offset:swizzle(BITMASK_PERM,"ppiip")
	ds_swizzle_b32 v95, v93 offset:swizzle(BITMASK_PERM,"ppiip")
	ds_bpermute_b32 v89, v74, v4
	v_readlane_b32 s35, v4, s21
	v_readlane_b32 s36, v4, s15
	ds_swizzle_b32 v96, v92 offset:swizzle(BITMASK_PERM,"ppiip")
	ds_swizzle_b32 v97, v79 offset:swizzle(BITMASK_PERM,"ppiip")
	ds_swizzle_b32 v98, v56 offset:swizzle(BITMASK_PERM,"ppiip")
	ds_swizzle_b32 v99, v57 offset:swizzle(BITMASK_PERM,"ppiip")
	ds_swizzle_b32 v100, v60 offset:swizzle(BITMASK_PERM,"ppiip")
	ds_swizzle_b32 v101, v61 offset:swizzle(BITMASK_PERM,"ppiip")
	ds_swizzle_b32 v102, v88 offset:swizzle(BITMASK_PERM,"ppiip")
	ds_swizzle_b32 v103, v87 offset:swizzle(BITMASK_PERM,"ppiip")
	ds_swizzle_b32 v104, v83 offset:swizzle(BITMASK_PERM,"ppiip")
	ds_swizzle_b32 v105, v80 offset:swizzle(BITMASK_PERM,"ppiip")
	s_waitcnt lgkmcnt(9)
	v_fma_f32 v79, v89, v96, v79
	s_waitcnt lgkmcnt(8)
	v_fma_f32 v92, -v89, v97, v92
	v_fma_f32 v86, v89, v86, v93
	v_fma_f32 v93, -v89, v95, v94
	v_fma_f32 v62, v89, v84, v62
	v_fma_f32 v63, -v89, v85, v63
	v_fma_f32 v55, v89, v81, v55
	v_fma_f32 v58, -v89, v82, v58
	s_waitcnt lgkmcnt(1)
	v_fma_f32 v80, v89, v104, v80
	s_waitcnt lgkmcnt(0)
	v_fma_f32 v81, -v89, v105, v83
	v_fma_f32 v82, v89, v102, v87
	v_fma_f32 v83, -v89, v103, v88
	v_fma_f32 v61, v89, v100, v61
	v_fma_f32 v60, -v89, v101, v60
	v_fma_f32 v57, v89, v98, v57
	v_fma_f32 v56, -v89, v99, v56
	v_mul_f32 v84, v112, v58
	v_mul_f32 v85, v112, v55
	v_mul_f32 v87, v64, v63
	v_mul_f32 v88, v64, v62
	v_mul_f32 v95, v64, v92
	v_mul_f32 v64, v64, v79
	v_mov_b32_e32 v69, s35
	v_mov_b32_e32 v70, s36
	v_mul_f32 v89, v112, v93
	v_mul_f32 v94, v112, v86
	v_fma_f32 v55, -v113, v55, v84
	v_fma_f32 v58, v113, v58, v85
	v_fma_f32 v62, -v90, v62, v87
	v_fma_f32 v63, v90, v63, v88
	v_mul_f32 v84, v114, v56
	v_mul_f32 v85, v114, v57
	v_mul_f32 v87, v66, v60
	v_mul_f32 v88, v66, v61
	v_mul_f32 v96, v114, v83
	v_mul_f32 v97, v114, v82
	v_mul_f32 v98, v66, v81
	v_mul_f32 v66, v66, v80
	v_fma_f32 v86, -v113, v86, v89
	v_fma_f32 v79, -v90, v79, v95
	v_fma_f32 v64, v90, v92, v64
	v_fma_f32 v57, -v59, v57, v84
	v_fma_f32 v56, v59, v56, v85
	v_fma_f32 v61, -v65, v61, v87
	v_fma_f32 v60, v65, v60, v88
	v_fma_f32 v82, -v59, v82, v96
	v_fma_f32 v59, v59, v83, v97
	v_fma_f32 v80, -v65, v80, v98
	v_fma_f32 v65, v65, v81, v66
	ds_bpermute_b32 v75, v75, v4
	v_fma_f32 v89, v113, v93, v94
	v_fma_f32 v66, v69, v82, v64
	v_fma_f32 v81, -v69, v59, v79
	v_fma_f32 v84, -v70, v65, v86
	v_fma_f32 v65, v70, v86, v65
	v_fma_f32 v59, v69, v79, v59
	v_fma_f32 v83, v70, v80, v89
	v_fma_f32 v80, -v70, v89, v80
	v_fma_f32 v64, -v69, v64, v82
	v_fma_f32 v79, v69, v55, v60
	v_fma_f32 v82, -v69, v58, v61
	v_fma_f32 v85, v70, v62, v56
	v_fma_f32 v86, -v70, v63, v57
	v_fma_f32 v57, v70, v57, v63
	v_fma_f32 v56, -v70, v56, v62
	v_fma_f32 v58, v69, v61, v58
	v_fma_f32 v55, -v69, v60, v55
	ds_bpermute_b32 v60, v20, v55
	ds_bpermute_b32 v61, v20, v58
	ds_bpermute_b32 v62, v20, v56
	ds_bpermute_b32 v63, v20, v57
	ds_bpermute_b32 v69, v20, v86
	ds_bpermute_b32 v70, v20, v85
	ds_bpermute_b32 v87, v20, v82
	ds_bpermute_b32 v92, v20, v80
	ds_bpermute_b32 v88, v20, v79
	ds_bpermute_b32 v89, v20, v64
	ds_bpermute_b32 v90, v20, v59
	ds_bpermute_b32 v93, v20, v81
	ds_bpermute_b32 v94, v20, v66
	ds_bpermute_b32 v95, v20, v84
	ds_bpermute_b32 v96, v20, v83
	ds_bpermute_b32 v97, v20, v65
	s_waitcnt lgkmcnt(4)
	v_fma_f32 v66, v75, v93, v66
	s_waitcnt lgkmcnt(3)
	v_fma_f32 v81, -v75, v94, v81
	s_waitcnt lgkmcnt(2)
	v_fma_f32 v83, v75, v95, v83
	s_waitcnt lgkmcnt(1)
	v_fma_f32 v84, -v75, v96, v84
	v_fma_f32 v65, v75, v92, v65
	s_waitcnt lgkmcnt(0)
	v_fma_f32 v80, -v75, v97, v80
	v_fma_f32 v59, v75, v89, v59
	v_fma_f32 v64, -v75, v90, v64
	v_fma_f32 v79, v75, v87, v79
	v_fma_f32 v82, -v75, v88, v82
	v_fma_f32 v69, v75, v69, v85
	v_fma_f32 v70, -v75, v70, v86
	v_fma_f32 v57, v75, v62, v57
	v_fma_f32 v56, -v75, v63, v56
	v_fma_f32 v58, v75, v60, v58
	v_fma_f32 v55, -v75, v61, v55
	ds_swizzle_b32 v60, v55 offset:swizzle(BITMASK_PERM,"piipp")
	ds_swizzle_b32 v61, v58 offset:swizzle(BITMASK_PERM,"piipp")
	ds_swizzle_b32 v62, v56 offset:swizzle(BITMASK_PERM,"piipp")
	ds_swizzle_b32 v63, v57 offset:swizzle(BITMASK_PERM,"piipp")
	ds_swizzle_b32 v75, v70 offset:swizzle(BITMASK_PERM,"piipp")
	ds_swizzle_b32 v85, v69 offset:swizzle(BITMASK_PERM,"piipp")
	ds_swizzle_b32 v86, v82 offset:swizzle(BITMASK_PERM,"piipp")
	ds_swizzle_b32 v87, v79 offset:swizzle(BITMASK_PERM,"piipp")
	ds_swizzle_b32 v92, v81 offset:swizzle(BITMASK_PERM,"piipp")
	ds_bpermute_b32 v76, v76, v4
	ds_swizzle_b32 v88, v64 offset:swizzle(BITMASK_PERM,"piipp")
	ds_swizzle_b32 v89, v59 offset:swizzle(BITMASK_PERM,"piipp")
	ds_swizzle_b32 v90, v80 offset:swizzle(BITMASK_PERM,"piipp")
	ds_swizzle_b32 v93, v66 offset:swizzle(BITMASK_PERM,"piipp")
	ds_swizzle_b32 v94, v84 offset:swizzle(BITMASK_PERM,"piipp")
	ds_swizzle_b32 v95, v83 offset:swizzle(BITMASK_PERM,"piipp")
	ds_bpermute_b32 v77, v77, v4
	ds_swizzle_b32 v96, v65 offset:swizzle(BITMASK_PERM,"piipp")
	s_waitcnt lgkmcnt(8)
	v_fma_f32 v66, v76, v92, v66
	s_waitcnt lgkmcnt(4)
	v_fma_f32 v81, -v76, v93, v81
	s_waitcnt lgkmcnt(3)
	v_fma_f32 v83, v76, v94, v83
	s_waitcnt lgkmcnt(2)
	v_fma_f32 v84, -v76, v95, v84
	v_fma_f32 v65, v76, v90, v65
	s_waitcnt lgkmcnt(0)
	v_fma_f32 v80, -v76, v96, v80
	v_fma_f32 v59, v76, v88, v59
	v_fma_f32 v64, -v76, v89, v64
	v_fma_f32 v79, v76, v86, v79
	v_fma_f32 v82, -v76, v87, v82
	v_fma_f32 v69, v76, v75, v69
	v_fma_f32 v70, -v76, v85, v70
	v_fma_f32 v57, v76, v62, v57
	v_fma_f32 v56, -v76, v63, v56
	v_fma_f32 v58, v76, v60, v58
	v_fma_f32 v55, -v76, v61, v55
	s_nop 1
	v_mov_b32_dpp v85, v82 quad_perm:[3,2,1,0] row_mask:0xf bank_mask:0xf bound_ctrl:1
	v_mov_b32_dpp v75, v70 quad_perm:[3,2,1,0] row_mask:0xf bank_mask:0xf bound_ctrl:1
	v_mov_b32_dpp v60, v55 quad_perm:[3,2,1,0] row_mask:0xf bank_mask:0xf bound_ctrl:1
	v_mov_b32_dpp v61, v58 quad_perm:[3,2,1,0] row_mask:0xf bank_mask:0xf bound_ctrl:1
	v_mov_b32_dpp v62, v56 quad_perm:[3,2,1,0] row_mask:0xf bank_mask:0xf bound_ctrl:1
	v_mov_b32_dpp v63, v57 quad_perm:[3,2,1,0] row_mask:0xf bank_mask:0xf bound_ctrl:1
	v_mov_b32_dpp v86, v79 quad_perm:[3,2,1,0] row_mask:0xf bank_mask:0xf bound_ctrl:1
	v_mov_b32_dpp v87, v64 quad_perm:[3,2,1,0] row_mask:0xf bank_mask:0xf bound_ctrl:1
	v_mov_b32_dpp v92, v84 quad_perm:[3,2,1,0] row_mask:0xf bank_mask:0xf bound_ctrl:1
	v_mov_b32_dpp v76, v69 quad_perm:[3,2,1,0] row_mask:0xf bank_mask:0xf bound_ctrl:1
	v_mov_b32_dpp v88, v59 quad_perm:[3,2,1,0] row_mask:0xf bank_mask:0xf bound_ctrl:1
	v_mov_b32_dpp v89, v80 quad_perm:[3,2,1,0] row_mask:0xf bank_mask:0xf bound_ctrl:1
	v_mov_b32_dpp v90, v65 quad_perm:[3,2,1,0] row_mask:0xf bank_mask:0xf bound_ctrl:1
	v_mov_b32_dpp v93, v83 quad_perm:[3,2,1,0] row_mask:0xf bank_mask:0xf bound_ctrl:1
	v_mov_b32_dpp v94, v81 quad_perm:[3,2,1,0] row_mask:0xf bank_mask:0xf bound_ctrl:1
	v_mov_b32_dpp v95, v66 quad_perm:[3,2,1,0] row_mask:0xf bank_mask:0xf bound_ctrl:1
	v_fma_f32 v66, v77, v94, v66
	v_fma_f32 v81, -v77, v95, v81
	v_fma_f32 v83, v77, v92, v83
	v_fma_f32 v84, -v77, v93, v84
	v_fma_f32 v65, v77, v89, v65
	v_fma_f32 v80, -v77, v90, v80
	v_fma_f32 v59, v77, v87, v59
	v_fma_f32 v64, -v77, v88, v64
	v_fma_f32 v79, v77, v85, v79
	v_fma_f32 v82, -v77, v86, v82
	v_fma_f32 v69, v77, v75, v69
	v_fma_f32 v70, -v77, v76, v70
	v_fma_f32 v57, v77, v62, v57
	v_fma_f32 v56, -v77, v63, v56
	v_fma_f32 v58, v77, v60, v58
	v_fma_f32 v55, -v77, v61, v55
	v_mul_f32 v77, v67, v82
	v_mul_f32 v75, v91, v70
	v_mul_f32 v63, v91, v57
	v_mul_f32 v62, v91, v56
	v_mul_f32 v61, v67, v58
	v_mul_f32 v60, v67, v55
	v_mul_f32 v85, v67, v79
	v_mul_f32 v86, v67, v64
	v_mul_f32 v87, v67, v59
	v_mul_f32 v92, v67, v81
	v_mul_f32 v67, v67, v66
	v_mul_f32 v76, v91, v69
	v_mul_f32 v88, v91, v80
	v_mul_f32 v89, v91, v65
	v_mul_f32 v90, v91, v84
	v_mul_f32 v91, v91, v83
	v_fma_f32 v58, -v68, v58, v60
	v_fma_f32 v55, v68, v55, v61
	v_fma_f32 v57, -v78, v57, v62
	v_fma_f32 v56, v78, v56, v63
	v_fma_f32 v60, -v78, v69, v75
	v_fma_f32 v61, v78, v70, v76
	v_fma_f32 v62, -v68, v79, v77
	v_fma_f32 v63, v68, v82, v85
	v_fma_f32 v59, -v68, v59, v86
	v_fma_f32 v64, v68, v64, v87
	v_fma_f32 v65, -v78, v65, v88
	v_fma_f32 v69, v78, v80, v89
	v_fma_f32 v70, -v78, v83, v90
	v_fma_f32 v75, v78, v84, v91
	v_fma_f32 v66, -v68, v66, v92
	v_fma_f32 v67, v68, v81, v67
	s_nop 0
	s_nop 1
	v_fmac_f32_dpp v58, v58, v23 quad_perm:[1,0,3,2] row_mask:0xf bank_mask:0xf
	v_fmac_f32_dpp v57, v57, v23 quad_perm:[1,0,3,2] row_mask:0xf bank_mask:0xf
	v_fmac_f32_dpp v60, v60, v23 quad_perm:[1,0,3,2] row_mask:0xf bank_mask:0xf
	v_fmac_f32_dpp v62, v62, v23 quad_perm:[1,0,3,2] row_mask:0xf bank_mask:0xf
	v_fmac_f32_dpp v55, v55, v23 quad_perm:[1,0,3,2] row_mask:0xf bank_mask:0xf
	v_fmac_f32_dpp v56, v56, v23 quad_perm:[1,0,3,2] row_mask:0xf bank_mask:0xf
	v_fmac_f32_dpp v61, v61, v23 quad_perm:[1,0,3,2] row_mask:0xf bank_mask:0xf
	v_fmac_f32_dpp v63, v63, v23 quad_perm:[1,0,3,2] row_mask:0xf bank_mask:0xf

	s_or_b32 s18, s10, 4
	v_fmac_f32_dpp v59, v59, v23 quad_perm:[1,0,3,2] row_mask:0xf bank_mask:0xf
	v_fmac_f32_dpp v65, v65, v23 quad_perm:[1,0,3,2] row_mask:0xf bank_mask:0xf
	v_fmac_f32_dpp v70, v70, v23 quad_perm:[1,0,3,2] row_mask:0xf bank_mask:0xf
	v_fmac_f32_dpp v66, v66, v23 quad_perm:[1,0,3,2] row_mask:0xf bank_mask:0xf
	v_fmac_f32_dpp v64, v64, v23 quad_perm:[1,0,3,2] row_mask:0xf bank_mask:0xf
	v_fmac_f32_dpp v69, v69, v23 quad_perm:[1,0,3,2] row_mask:0xf bank_mask:0xf
	v_fmac_f32_dpp v75, v75, v23 quad_perm:[1,0,3,2] row_mask:0xf bank_mask:0xf
	v_fmac_f32_dpp v67, v67, v23 quad_perm:[1,0,3,2] row_mask:0xf bank_mask:0xf

	v_fmac_f32_dpp v58, v58, v24 quad_perm:[2,3,0,1] row_mask:0xf bank_mask:0xf
	v_fmac_f32_dpp v57, v57, v24 quad_perm:[2,3,0,1] row_mask:0xf bank_mask:0xf
	v_fmac_f32_dpp v60, v60, v24 quad_perm:[2,3,0,1] row_mask:0xf bank_mask:0xf
	v_fmac_f32_dpp v62, v62, v24 quad_perm:[2,3,0,1] row_mask:0xf bank_mask:0xf
	v_fmac_f32_dpp v55, v55, v24 quad_perm:[2,3,0,1] row_mask:0xf bank_mask:0xf
	v_fmac_f32_dpp v56, v56, v24 quad_perm:[2,3,0,1] row_mask:0xf bank_mask:0xf
	v_fmac_f32_dpp v61, v61, v24 quad_perm:[2,3,0,1] row_mask:0xf bank_mask:0xf
	v_fmac_f32_dpp v63, v63, v24 quad_perm:[2,3,0,1] row_mask:0xf bank_mask:0xf

	s_or_b32 s22, s10, 3
	v_fmac_f32_dpp v59, v59, v24 quad_perm:[2,3,0,1] row_mask:0xf bank_mask:0xf
	v_fmac_f32_dpp v65, v65, v24 quad_perm:[2,3,0,1] row_mask:0xf bank_mask:0xf
	v_fmac_f32_dpp v70, v70, v24 quad_perm:[2,3,0,1] row_mask:0xf bank_mask:0xf
	v_fmac_f32_dpp v66, v66, v24 quad_perm:[2,3,0,1] row_mask:0xf bank_mask:0xf
	v_fmac_f32_dpp v64, v64, v24 quad_perm:[2,3,0,1] row_mask:0xf bank_mask:0xf
	v_fmac_f32_dpp v69, v69, v24 quad_perm:[2,3,0,1] row_mask:0xf bank_mask:0xf
	v_fmac_f32_dpp v75, v75, v24 quad_perm:[2,3,0,1] row_mask:0xf bank_mask:0xf
	v_fmac_f32_dpp v67, v67, v24 quad_perm:[2,3,0,1] row_mask:0xf bank_mask:0xf

	v_readlane_b32 s19, v52, s18
	v_mov_b32_dpp v68, v58 row_half_mirror row_mask:0xf bank_mask:0xf bound_ctrl:1
	v_mov_b32_dpp v76, v57 row_half_mirror row_mask:0xf bank_mask:0xf bound_ctrl:1
	v_mov_b32_dpp v77, v60 row_half_mirror row_mask:0xf bank_mask:0xf bound_ctrl:1
	v_mov_b32_dpp v78, v62 row_half_mirror row_mask:0xf bank_mask:0xf bound_ctrl:1
	v_mov_b32_dpp v79, v55 row_half_mirror row_mask:0xf bank_mask:0xf bound_ctrl:1
	v_mov_b32_dpp v80, v56 row_half_mirror row_mask:0xf bank_mask:0xf bound_ctrl:1
	v_mov_b32_dpp v81, v61 row_half_mirror row_mask:0xf bank_mask:0xf bound_ctrl:1
	v_mov_b32_dpp v82, v63 row_half_mirror row_mask:0xf bank_mask:0xf bound_ctrl:1
	v_mov_b32_dpp v83, v59 row_half_mirror row_mask:0xf bank_mask:0xf bound_ctrl:1
	v_mov_b32_dpp v84, v65 row_half_mirror row_mask:0xf bank_mask:0xf bound_ctrl:1
	v_mov_b32_dpp v85, v70 row_half_mirror row_mask:0xf bank_mask:0xf bound_ctrl:1
	v_mov_b32_dpp v86, v66 row_half_mirror row_mask:0xf bank_mask:0xf bound_ctrl:1
	v_mov_b32_dpp v87, v64 row_half_mirror row_mask:0xf bank_mask:0xf bound_ctrl:1
	v_mov_b32_dpp v88, v69 row_half_mirror row_mask:0xf bank_mask:0xf bound_ctrl:1
	v_mov_b32_dpp v89, v75 row_half_mirror row_mask:0xf bank_mask:0xf bound_ctrl:1
	v_mov_b32_dpp v90, v67 row_half_mirror row_mask:0xf bank_mask:0xf bound_ctrl:1
	v_fmac_f32_dpp v58, v68, v25 quad_perm:[3,2,1,0] row_mask:0xf bank_mask:0xf
	v_fmac_f32_dpp v57, v76, v25 quad_perm:[3,2,1,0] row_mask:0xf bank_mask:0xf
	v_fmac_f32_dpp v60, v77, v25 quad_perm:[3,2,1,0] row_mask:0xf bank_mask:0xf
	v_fmac_f32_dpp v62, v78, v25 quad_perm:[3,2,1,0] row_mask:0xf bank_mask:0xf
	v_fmac_f32_dpp v55, v79, v25 quad_perm:[3,2,1,0] row_mask:0xf bank_mask:0xf
	v_fmac_f32_dpp v56, v80, v25 quad_perm:[3,2,1,0] row_mask:0xf bank_mask:0xf
	v_fmac_f32_dpp v61, v81, v25 quad_perm:[3,2,1,0] row_mask:0xf bank_mask:0xf
	v_fmac_f32_dpp v63, v82, v25 quad_perm:[3,2,1,0] row_mask:0xf bank_mask:0xf

	v_fmac_f32_dpp v59, v83, v25 quad_perm:[3,2,1,0] row_mask:0xf bank_mask:0xf
	v_fmac_f32_dpp v65, v84, v25 quad_perm:[3,2,1,0] row_mask:0xf bank_mask:0xf
	v_fmac_f32_dpp v70, v85, v25 quad_perm:[3,2,1,0] row_mask:0xf bank_mask:0xf
	v_fmac_f32_dpp v66, v86, v25 quad_perm:[3,2,1,0] row_mask:0xf bank_mask:0xf
	v_fmac_f32_dpp v64, v87, v25 quad_perm:[3,2,1,0] row_mask:0xf bank_mask:0xf
	v_fmac_f32_dpp v69, v88, v25 quad_perm:[3,2,1,0] row_mask:0xf bank_mask:0xf
	v_fmac_f32_dpp v75, v89, v25 quad_perm:[3,2,1,0] row_mask:0xf bank_mask:0xf
	v_fmac_f32_dpp v67, v90, v25 quad_perm:[3,2,1,0] row_mask:0xf bank_mask:0xf

	v_readlane_b32 s18, v52, s22
	s_nop 1
	v_fmac_f32_dpp v58, v58, v26 row_ror:8 row_mask:0xf bank_mask:0xf
	v_fmac_f32_dpp v57, v57, v26 row_ror:8 row_mask:0xf bank_mask:0xf
	v_fmac_f32_dpp v60, v60, v26 row_ror:8 row_mask:0xf bank_mask:0xf
	v_fmac_f32_dpp v62, v62, v26 row_ror:8 row_mask:0xf bank_mask:0xf
	v_fmac_f32_dpp v55, v55, v26 row_ror:8 row_mask:0xf bank_mask:0xf
	v_fmac_f32_dpp v56, v56, v26 row_ror:8 row_mask:0xf bank_mask:0xf
	v_fmac_f32_dpp v61, v61, v26 row_ror:8 row_mask:0xf bank_mask:0xf
	v_fmac_f32_dpp v63, v63, v26 row_ror:8 row_mask:0xf bank_mask:0xf

	v_fmac_f32_dpp v59, v59, v26 row_ror:8 row_mask:0xf bank_mask:0xf
	v_fmac_f32_dpp v65, v65, v26 row_ror:8 row_mask:0xf bank_mask:0xf
	v_fmac_f32_dpp v70, v70, v26 row_ror:8 row_mask:0xf bank_mask:0xf
	v_fmac_f32_dpp v66, v66, v26 row_ror:8 row_mask:0xf bank_mask:0xf
	v_fmac_f32_dpp v64, v64, v26 row_ror:8 row_mask:0xf bank_mask:0xf
	v_fmac_f32_dpp v69, v69, v26 row_ror:8 row_mask:0xf bank_mask:0xf
	v_fmac_f32_dpp v75, v75, v26 row_ror:8 row_mask:0xf bank_mask:0xf
	v_fmac_f32_dpp v67, v67, v26 row_ror:8 row_mask:0xf bank_mask:0xf

	s_or_b32 s23, s10, 2
	v_add_f32 v68, v58, v57
	v_sub_f32 v57, v58, v57
	v_add_f32 v58, v55, v56
	v_sub_f32 v55, v55, v56
	v_add_f32 v56, v60, v62
	v_sub_f32 v60, v60, v62
	v_add_f32 v62, v61, v63
	v_sub_f32 v61, v61, v63
	v_add_f32 v63, v59, v65
	v_sub_f32 v59, v59, v65
	v_add_f32 v65, v64, v69
	v_sub_f32 v64, v64, v69
	v_add_f32 v69, v70, v66
	v_sub_f32 v66, v70, v66
	v_add_f32 v70, v75, v67
	v_sub_f32 v67, v75, v67
	v_add_f32 v75, v68, v56
	v_sub_f32 v56, v68, v56
	v_add_f32 v68, v58, v62
	v_sub_f32 v58, v58, v62
	v_add_f32 v62, v57, v60
	v_sub_f32 v57, v57, v60
	v_add_f32 v60, v55, v61
	v_sub_f32 v55, v55, v61
	v_add_f32 v61, v63, v69
	v_sub_f32 v63, v63, v69
	v_add_f32 v69, v65, v70
	v_sub_f32 v65, v65, v70
	v_add_f32 v70, v59, v66
	v_sub_f32 v59, v59, v66
	v_add_f32 v66, v64, v67
	v_sub_f32 v64, v64, v67
	v_add_f32 v67, v75, v61
	v_sub_f32 v61, v75, v61
	v_add_f32 v75, v68, v69
	v_sub_f32 v68, v68, v69
	v_add_f32 v69, v62, v70
	v_sub_f32 v62, v62, v70
	v_add_f32 v70, v60, v66
	v_sub_f32 v60, v60, v66
	v_add_f32 v66, v56, v63
	v_sub_f32 v56, v56, v63
	v_add_f32 v63, v58, v65
	v_sub_f32 v58, v58, v65
	v_add_f32 v65, v57, v59
	v_sub_f32 v57, v57, v59
	v_add_f32 v59, v55, v64
	v_sub_f32 v55, v55, v64
	v_readlane_b32 s15, v52, s23
	s_nop 1
	v_permlane16_swap_b32 v67, v69
	v_permlane16_swap_b32 v75, v70
	v_permlane16_swap_b32 v66, v65
	v_permlane16_swap_b32 v63, v59
	v_permlane16_swap_b32 v61, v62
	v_permlane16_swap_b32 v68, v60
	v_permlane16_swap_b32 v56, v57
	v_permlane16_swap_b32 v58, v55
	s_or_b32 s24, s10, 5
	v_permlane32_swap_b32 v67, v66
	v_permlane32_swap_b32 v75, v63
	v_permlane32_swap_b32 v69, v65
	v_permlane32_swap_b32 v70, v59
	v_permlane32_swap_b32 v61, v56
	v_permlane32_swap_b32 v68, v58
	v_permlane32_swap_b32 v62, v57
	v_permlane32_swap_b32 v60, v55
	v_readlane_b32 s11, v52, s20
	v_add_f32 v64, v67, v69
	v_sub_f32 v67, v67, v69
	v_add_f32 v69, v75, v70
	v_sub_f32 v70, v75, v70
	v_add_f32 v75, v66, v65
	v_sub_f32 v65, v66, v65
	v_add_f32 v66, v63, v59
	v_sub_f32 v59, v63, v59
	v_add_f32 v63, v61, v62
	v_sub_f32 v61, v61, v62
	v_add_f32 v62, v68, v60
	v_sub_f32 v60, v68, v60
	v_add_f32 v68, v56, v57
	v_sub_f32 v56, v56, v57
	v_add_f32 v57, v58, v55
	v_sub_f32 v55, v58, v55
	v_add_f32 v58, v64, v75
	v_sub_f32 v64, v64, v75
	v_add_f32 v75, v69, v66
	v_sub_f32 v66, v69, v66
	v_add_f32 v69, v67, v65
	v_sub_f32 v65, v67, v65
	v_add_f32 v67, v70, v59
	v_sub_f32 v59, v70, v59
	v_add_f32 v70, v63, v68
	v_sub_f32 v63, v63, v68
	v_add_f32 v68, v62, v57
	v_sub_f32 v57, v62, v57
	v_add_f32 v62, v61, v56
	v_sub_f32 v56, v61, v56
	v_add_f32 v61, v60, v55
	v_sub_f32 v55, v60, v55
	v_mul_f32 v58, v58, v11
	v_mul_f32 v60, v75, v11
	v_mul_f32 v69, v69, v12
	v_mul_f32 v67, v67, v12
	v_mul_f32 v64, v64, v13
	v_mul_f32 v66, v66, v13
	v_mul_f32 v65, v65, v14
	v_mul_f32 v59, v59, v14
	v_mul_f32 v70, v70, v15
	v_mul_f32 v68, v68, v15
	v_mul_f32 v62, v62, v16
	v_mul_f32 v61, v61, v16
	v_mul_f32 v56, v56, v18
	v_mul_f32 v55, v55, v18
	v_mul_f32 v63, v63, v17
	v_mul_f32 v57, v57, v17
	s_nop 0
	v_fma_f32 v75, s19, v67, v58
	v_fma_f32 v76, -s19, v69, v60
	v_fma_f32 v60, s19, v60, v69
	v_fma_f32 v58, -s19, v58, v67
	v_fma_f32 v67, s19, v59, v64
	v_fma_f32 v69, -s19, v65, v66
	v_fma_f32 v65, s19, v66, v65
	v_fma_f32 v59, -s19, v64, v59
	v_fma_f32 v64, s19, v61, v70
	v_fma_f32 v66, -s19, v62, v68
	v_fma_f32 v62, s19, v68, v62
	v_fma_f32 v61, -s19, v70, v61
	v_fma_f32 v68, s19, v55, v63
	v_fma_f32 v70, -s19, v56, v57
	v_fma_f32 v56, s19, v57, v56
	v_fma_f32 v55, -s19, v63, v55
	s_nop 0
	v_fma_f32 v57, s18, v69, v75
	v_fma_f32 v63, -s18, v67, v76
	v_fma_f32 v67, s18, v76, v67
	v_fma_f32 v69, -s18, v75, v69
	v_fma_f32 v75, s18, v59, v60
	v_fma_f32 v76, -s18, v65, v58
	v_fma_f32 v58, s18, v58, v65
	v_fma_f32 v59, -s18, v60, v59
	v_fma_f32 v60, s18, v70, v64
	v_fma_f32 v65, -s18, v68, v66
	v_fma_f32 v66, s18, v66, v68
	v_fma_f32 v64, -s18, v64, v70
	v_fma_f32 v68, s18, v55, v62
	v_fma_f32 v70, -s18, v56, v61
	v_fma_f32 v56, s18, v61, v56
	v_fma_f32 v55, -s18, v62, v55
	s_nop 0
	s_nop 1
	v_permlane32_swap_b32 v57, v67
	v_permlane32_swap_b32 v63, v69
	v_permlane32_swap_b32 v75, v58
	v_permlane32_swap_b32 v76, v59
	s_or_b32 s25, s10, 6
	v_permlane32_swap_b32 v60, v66
	v_permlane32_swap_b32 v65, v64
	v_permlane32_swap_b32 v68, v56
	v_permlane32_swap_b32 v70, v55
	v_permlane16_swap_b32 v57, v75
	v_permlane16_swap_b32 v63, v76
	v_permlane16_swap_b32 v67, v58
	v_permlane16_swap_b32 v69, v59
	s_or_b32 s26, s10, 7
	v_permlane16_swap_b32 v60, v68
	v_permlane16_swap_b32 v65, v70
	v_permlane16_swap_b32 v66, v56
	v_permlane16_swap_b32 v64, v55
	v_fma_f32 v61, s15, v76, v57
	v_fma_f32 v62, -s15, v75, v63
	v_fma_f32 v63, s15, v63, v75
	v_fma_f32 v57, -s15, v57, v76
	v_fma_f32 v75, s15, v59, v67
	v_fma_f32 v76, -s15, v58, v69
	v_fma_f32 v58, s15, v69, v58
	v_fma_f32 v59, -s15, v67, v59
	s_nop 0
	v_fma_f32 v67, s15, v70, v60
	v_fma_f32 v69, -s15, v68, v65
	v_fma_f32 v60, -s15, v60, v70
	v_fma_f32 v70, -s15, v56, v64
	v_fma_f32 v65, s15, v65, v68
	v_fma_f32 v68, s15, v55, v66
	v_fma_f32 v56, s15, v64, v56
	v_fma_f32 v55, -s15, v66, v55
	v_fma_f32 v64, s11, v76, v61
	v_fma_f32 v77, -s11, v75, v62
	v_fma_f32 v75, s11, v62, v75
	v_fma_f32 v61, -s11, v61, v76
	v_fma_f32 v76, s11, v59, v63
	v_fma_f32 v62, -s11, v58, v57
	v_fma_f32 v78, s11, v57, v58
	v_fma_f32 v79, -s11, v63, v59
	s_nop 0
	v_fma_f32 v57, s11, v70, v67
	v_fma_f32 v59, -s11, v68, v69
	v_fma_f32 v69, s11, v69, v68
	v_fma_f32 v70, -s11, v67, v70
	v_fma_f32 v63, s11, v55, v65
	v_readlane_b32 s10, v52, s10
	v_readlane_b32 s20, v52, s24
	v_fma_f32 v80, -s11, v56, v60
	v_fma_f32 v81, s11, v60, v56
	v_fma_f32 v82, -s11, v65, v55
	v_fma_f32 v65, s10, v59, v64
	v_fma_f32 v66, -s10, v57, v77
	v_fma_f32 v58, s10, v77, v57
	v_fma_f32 v59, -s10, v64, v59
	s_nop 0
	v_fma_f32 v67, s10, v80, v76
	v_fma_f32 v68, -s10, v63, v62
	v_fma_f32 v62, s10, v62, v63
	v_fma_f32 v63, -s10, v76, v80
	v_fma_f32 v56, s10, v70, v75
	v_fma_f32 v57, -s10, v69, v61
	v_fma_f32 v55, s10, v61, v69
	v_fma_f32 v64, -s10, v75, v70
	v_fma_f32 v60, s10, v82, v78
	v_fma_f32 v61, -s10, v81, v79
	v_fma_f32 v69, s10, v79, v81
	v_fma_f32 v70, -s10, v78, v82
	s_nop 0
	v_mov_b32_e32 v74, s20
	s_nop 1
	v_mul_f32_dpp v75, v65, v74 row_ror:8 row_mask:0xf bank_mask:0xf
	v_mul_f32_dpp v76, v67, v74 row_ror:8 row_mask:0xf bank_mask:0xf
	v_mul_f32_dpp v77, v56, v74 row_ror:8 row_mask:0xf bank_mask:0xf
	v_mul_f32_dpp v78, v60, v74 row_ror:8 row_mask:0xf bank_mask:0xf
	v_fmac_f32_dpp v65, v66, v74 row_ror:8 row_mask:0xf bank_mask:0xf
	v_fmac_f32_dpp v67, v68, v74 row_ror:8 row_mask:0xf bank_mask:0xf
	v_fmac_f32_dpp v56, v57, v74 row_ror:8 row_mask:0xf bank_mask:0xf
	v_fmac_f32_dpp v60, v61, v74 row_ror:8 row_mask:0xf bank_mask:0xf
	v_sub_f32 v66, v66, v75
	v_sub_f32 v68, v68, v76
	v_sub_f32 v57, v57, v77
	v_sub_f32 v61, v61, v78
	v_readlane_b32 s22, v52, s25
	s_nop 1
	v_mul_f32_dpp v75, v58, v74 row_ror:8 row_mask:0xf bank_mask:0xf
	v_mul_f32_dpp v76, v62, v74 row_ror:8 row_mask:0xf bank_mask:0xf
	v_mul_f32_dpp v77, v55, v74 row_ror:8 row_mask:0xf bank_mask:0xf
	v_mul_f32_dpp v78, v69, v74 row_ror:8 row_mask:0xf bank_mask:0xf
	v_fmac_f32_dpp v58, v59, v74 row_ror:8 row_mask:0xf bank_mask:0xf
	v_fmac_f32_dpp v62, v63, v74 row_ror:8 row_mask:0xf bank_mask:0xf
	v_fmac_f32_dpp v55, v64, v74 row_ror:8 row_mask:0xf bank_mask:0xf
	v_fmac_f32_dpp v69, v70, v74 row_ror:8 row_mask:0xf bank_mask:0xf
	v_sub_f32 v59, v59, v75
	v_sub_f32 v63, v63, v76
	v_sub_f32 v64, v64, v77
	v_sub_f32 v70, v70, v78
	v_readlane_b32 s23, v52, s26
	v_mov_b32_dpp v74, v65 row_half_mirror row_mask:0xf bank_mask:0xf bound_ctrl:1
	v_mov_b32_dpp v75, v67 row_half_mirror row_mask:0xf bank_mask:0xf bound_ctrl:1
	v_mov_b32_dpp v76, v56 row_half_mirror row_mask:0xf bank_mask:0xf bound_ctrl:1
	v_mov_b32_dpp v77, v60 row_half_mirror row_mask:0xf bank_mask:0xf bound_ctrl:1
	v_mov_b32_e32 v73, s22
	v_mov_b32_dpp v78, v66 row_half_mirror row_mask:0xf bank_mask:0xf bound_ctrl:1
	v_mov_b32_dpp v79, v68 row_half_mirror row_mask:0xf bank_mask:0xf bound_ctrl:1
	v_mov_b32_dpp v80, v57 row_half_mirror row_mask:0xf bank_mask:0xf bound_ctrl:1
	v_mov_b32_dpp v81, v61 row_half_mirror row_mask:0xf bank_mask:0xf bound_ctrl:1
	v_mov_b32_dpp v82, v58 row_half_mirror row_mask:0xf bank_mask:0xf bound_ctrl:1
	v_mov_b32_dpp v83, v62 row_half_mirror row_mask:0xf bank_mask:0xf bound_ctrl:1
	v_mov_b32_dpp v84, v55 row_half_mirror row_mask:0xf bank_mask:0xf bound_ctrl:1
	v_mov_b32_dpp v85, v69 row_half_mirror row_mask:0xf bank_mask:0xf bound_ctrl:1
	v_mov_b32_dpp v86, v59 row_half_mirror row_mask:0xf bank_mask:0xf bound_ctrl:1
	v_mov_b32_dpp v87, v63 row_half_mirror row_mask:0xf bank_mask:0xf bound_ctrl:1
	v_mov_b32_dpp v88, v64 row_half_mirror row_mask:0xf bank_mask:0xf bound_ctrl:1
	v_mov_b32_dpp v89, v70 row_half_mirror row_mask:0xf bank_mask:0xf bound_ctrl:1
	v_mul_f32_dpp v90, v74, v73 quad_perm:[3,2,1,0] row_mask:0xf bank_mask:0xf
	v_mul_f32_dpp v91, v75, v73 quad_perm:[3,2,1,0] row_mask:0xf bank_mask:0xf
	v_mul_f32_dpp v92, v76, v73 quad_perm:[3,2,1,0] row_mask:0xf bank_mask:0xf
	v_mul_f32_dpp v93, v77, v73 quad_perm:[3,2,1,0] row_mask:0xf bank_mask:0xf
	v_fmac_f32_dpp v65, v78, v73 quad_perm:[3,2,1,0] row_mask:0xf bank_mask:0xf
	v_fmac_f32_dpp v67, v79, v73 quad_perm:[3,2,1,0] row_mask:0xf bank_mask:0xf
	v_fmac_f32_dpp v56, v80, v73 quad_perm:[3,2,1,0] row_mask:0xf bank_mask:0xf
	v_fmac_f32_dpp v60, v81, v73 quad_perm:[3,2,1,0] row_mask:0xf bank_mask:0xf
	v_sub_f32 v66, v66, v90
	v_sub_f32 v68, v68, v91
	v_sub_f32 v57, v57, v92
	v_sub_f32 v61, v61, v93
	v_mul_f32_dpp v74, v82, v73 quad_perm:[3,2,1,0] row_mask:0xf bank_mask:0xf
	v_mul_f32_dpp v75, v83, v73 quad_perm:[3,2,1,0] row_mask:0xf bank_mask:0xf
	v_mul_f32_dpp v76, v84, v73 quad_perm:[3,2,1,0] row_mask:0xf bank_mask:0xf
	v_mul_f32_dpp v77, v85, v73 quad_perm:[3,2,1,0] row_mask:0xf bank_mask:0xf
	v_fmac_f32_dpp v58, v86, v73 quad_perm:[3,2,1,0] row_mask:0xf bank_mask:0xf
	v_fmac_f32_dpp v62, v87, v73 quad_perm:[3,2,1,0] row_mask:0xf bank_mask:0xf
	v_fmac_f32_dpp v55, v88, v73 quad_perm:[3,2,1,0] row_mask:0xf bank_mask:0xf
	v_fmac_f32_dpp v69, v89, v73 quad_perm:[3,2,1,0] row_mask:0xf bank_mask:0xf
	v_sub_f32 v59, v59, v74
	v_sub_f32 v63, v63, v75
	v_sub_f32 v64, v64, v76
	v_sub_f32 v70, v70, v77
	s_mov_b64 s[8:9], 0
	s_mov_b32 s14, 1
	v_readlane_b32 s21, v52, s21
	s_and_b64 vcc, exec, vcc
	v_mov_b32_e32 v72, s23
	s_nop 1
	v_mul_f32_dpp v73, v65, v72 quad_perm:[2,3,0,1] row_mask:0xf bank_mask:0xf
	v_mul_f32_dpp v74, v67, v72 quad_perm:[2,3,0,1] row_mask:0xf bank_mask:0xf
	v_mul_f32_dpp v75, v56, v72 quad_perm:[2,3,0,1] row_mask:0xf bank_mask:0xf
	v_mul_f32_dpp v76, v60, v72 quad_perm:[2,3,0,1] row_mask:0xf bank_mask:0xf
	v_fmac_f32_dpp v65, v66, v72 quad_perm:[2,3,0,1] row_mask:0xf bank_mask:0xf
	v_fmac_f32_dpp v67, v68, v72 quad_perm:[2,3,0,1] row_mask:0xf bank_mask:0xf
	v_fmac_f32_dpp v56, v57, v72 quad_perm:[2,3,0,1] row_mask:0xf bank_mask:0xf
	v_fmac_f32_dpp v60, v61, v72 quad_perm:[2,3,0,1] row_mask:0xf bank_mask:0xf
	v_sub_f32 v66, v66, v73
	v_sub_f32 v68, v68, v74
	v_sub_f32 v57, v57, v75
	v_sub_f32 v61, v61, v76
	v_mov_b32_e32 v71, s21
	v_mul_f32_dpp v73, v58, v72 quad_perm:[2,3,0,1] row_mask:0xf bank_mask:0xf
	v_mul_f32_dpp v74, v62, v72 quad_perm:[2,3,0,1] row_mask:0xf bank_mask:0xf
	v_mul_f32_dpp v75, v55, v72 quad_perm:[2,3,0,1] row_mask:0xf bank_mask:0xf
	v_mul_f32_dpp v76, v69, v72 quad_perm:[2,3,0,1] row_mask:0xf bank_mask:0xf
	v_fmac_f32_dpp v58, v59, v72 quad_perm:[2,3,0,1] row_mask:0xf bank_mask:0xf
	v_fmac_f32_dpp v62, v63, v72 quad_perm:[2,3,0,1] row_mask:0xf bank_mask:0xf
	v_fmac_f32_dpp v55, v64, v72 quad_perm:[2,3,0,1] row_mask:0xf bank_mask:0xf
	v_fmac_f32_dpp v69, v70, v72 quad_perm:[2,3,0,1] row_mask:0xf bank_mask:0xf
	v_sub_f32 v59, v59, v73
	v_sub_f32 v63, v63, v74
	v_sub_f32 v64, v64, v75
	v_sub_f32 v70, v70, v76
	s_nop 0
	s_nop 1
	v_mul_f32_dpp v72, v65, v71 quad_perm:[1,0,3,2] row_mask:0xf bank_mask:0xf
	v_mul_f32_dpp v73, v67, v71 quad_perm:[1,0,3,2] row_mask:0xf bank_mask:0xf
	v_mul_f32_dpp v74, v56, v71 quad_perm:[1,0,3,2] row_mask:0xf bank_mask:0xf
	v_mul_f32_dpp v75, v60, v71 quad_perm:[1,0,3,2] row_mask:0xf bank_mask:0xf
	v_fmac_f32_dpp v65, v66, v71 quad_perm:[1,0,3,2] row_mask:0xf bank_mask:0xf
	v_fmac_f32_dpp v67, v68, v71 quad_perm:[1,0,3,2] row_mask:0xf bank_mask:0xf
	v_fmac_f32_dpp v56, v57, v71 quad_perm:[1,0,3,2] row_mask:0xf bank_mask:0xf
	v_fmac_f32_dpp v60, v61, v71 quad_perm:[1,0,3,2] row_mask:0xf bank_mask:0xf
	v_sub_f32 v66, v66, v72
	v_sub_f32 v68, v68, v73
	v_sub_f32 v57, v57, v74
	v_sub_f32 v61, v61, v75
	s_nop 0
	s_nop 1
	v_mul_f32_dpp v72, v58, v71 quad_perm:[1,0,3,2] row_mask:0xf bank_mask:0xf
	v_mul_f32_dpp v73, v62, v71 quad_perm:[1,0,3,2] row_mask:0xf bank_mask:0xf
	v_mul_f32_dpp v74, v55, v71 quad_perm:[1,0,3,2] row_mask:0xf bank_mask:0xf
	v_mul_f32_dpp v75, v69, v71 quad_perm:[1,0,3,2] row_mask:0xf bank_mask:0xf
	v_fmac_f32_dpp v58, v59, v71 quad_perm:[1,0,3,2] row_mask:0xf bank_mask:0xf
	v_fmac_f32_dpp v62, v63, v71 quad_perm:[1,0,3,2] row_mask:0xf bank_mask:0xf
	v_fmac_f32_dpp v55, v64, v71 quad_perm:[1,0,3,2] row_mask:0xf bank_mask:0xf
	v_fmac_f32_dpp v69, v70, v71 quad_perm:[1,0,3,2] row_mask:0xf bank_mask:0xf
	v_sub_f32 v59, v59, v72
	v_sub_f32 v63, v63, v73
	v_sub_f32 v64, v64, v74
	v_sub_f32 v70, v70, v75
	s_cbranch_vccz .LBB0_24
	v_mul_f32_e32 v2, v53, v54
	v_mul_f32 v3, v65, v2
	v_mul_f32 v55, v57, v2
	v_mul_f32 v4, v66, v2
	v_mul_f32 v52, v67, v2
	v_mul_f32 v53, v68, v2
	v_mul_f32 v54, v56, v2
	v_mul_f32 v57, v3, v3
	v_mul_f32 v56, v60, v2
	v_mul_f32 v2, v61, v2
	s_mov_b64 s[10:11], 0
	v_fma_f32 v57, v4, v4, v57
	s_nop 0
	v_fma_f32 v57, v52, v52, v57
	s_nop 0
	v_fma_f32 v57, v53, v53, v57
	s_nop 0
	v_fma_f32 v57, v54, v54, v57
	s_nop 0
	v_fma_f32 v57, v55, v55, v57
	s_nop 0
	v_fma_f32 v57, v56, v56, v57
	s_nop 0
	v_fma_f32 v57, v2, v2, v57
	s_nop 1
	v_add_f32_dpp v57, v57, v57 quad_perm:[1,0,3,2] row_mask:0xf bank_mask:0xf bound_ctrl:1
	s_nop 1
	v_add_f32_dpp v57, v57, v57 quad_perm:[2,3,0,1] row_mask:0xf bank_mask:0xf bound_ctrl:1
	s_waitcnt lgkmcnt(0)
	s_nop 1
	v_add_f32_dpp v57, v57, v57 row_half_mirror row_mask:0xf bank_mask:0xf bound_ctrl:1
	s_nop 1
	v_add_f32_dpp v57, v57, v57 row_ror:8 row_mask:0xf bank_mask:0xf bound_ctrl:1
	v_mov_b32_e32 v58, v57
	s_nop 1
	v_permlane16_swap_b32 v58, v57
	s_waitcnt lgkmcnt(0)
	v_add_f32_e32 v57, v57, v58
	v_mov_b32_e32 v58, v57
	s_nop 1
	v_permlane32_swap_b32 v58, v57
	s_waitcnt lgkmcnt(0)
	v_add_f32_e32 v57, v57, v58
	v_mul_f32_e32 v58, 0x4f800000, v57
	v_cmp_gt_f32_e32 vcc, s17, v57
	s_nop 1
	v_cndmask_b32_e32 v57, v57, v58, vcc
	v_sqrt_f32_e32 v58, v57
	s_nop 0
	v_add_u32_e32 v59, -1, v58
	v_add_u32_e32 v60, 1, v58
	v_fma_f32 v61, -v59, v58, v57
	v_fma_f32 v62, -v60, v58, v57
	v_cmp_ge_f32_e64 s[8:9], 0, v61
	s_nop 1
	v_cndmask_b32_e64 v58, v58, v59, s[8:9]
	v_cmp_lt_f32_e64 s[8:9], 0, v62
	s_nop 1
	v_cndmask_b32_e64 v58, v58, v60, s[8:9]
	v_mul_f32_e32 v59, 0x37800000, v58
	v_cndmask_b32_e32 v58, v58, v59, vcc
	v_cmp_class_f32_e32 vcc, v57, v41
	s_nop 1
	v_cndmask_b32_e32 v57, v58, v57, vcc
	v_add_f32_e32 v57, 0x322bcc77, v57
	v_div_scale_f32 v58, s[8:9], v57, v57, 1.0
	v_rcp_f32_e32 v59, v58
	v_div_scale_f32 v60, vcc, 1.0, v57, 1.0
	v_fma_f32 v61, -v58, v59, 1.0
	v_fmac_f32_e32 v59, v61, v59
	v_mul_f32_e32 v61, v60, v59
	v_fma_f32 v62, -v58, v61, v60
	v_fmac_f32_e32 v61, v62, v59
	v_fma_f32 v58, -v58, v61, v60
	v_div_fmas_f32 v58, v58, v59, v61
	v_div_fixup_f32 v57, v58, v57, 1.0
	v_mul_f32 v3, v3, v57
	v_mul_f32 v4, v4, v57
	v_mul_f32 v52, v52, v57
	v_mul_f32 v53, v53, v57
	v_mul_f32 v2, v2, v57
	s_nop 0
	v_mul_f32 v58, v3, v42
	s_nop 0
	v_max_f32 v3, v3, v58
	v_mul_f32 v58, v4, v42
	s_nop 0
	v_max_f32 v4, v4, v58
	v_mul_f32 v58, v52, v42
	s_nop 0
	v_max_f32 v52, v52, v58
	v_mul_f32 v58, v53, v42
	s_nop 0
	v_max_f32 v58, v53, v58
	v_mul_f32 v53, v54, v57
	v_mul_f32 v54, v55, v57
	s_nop 0
	v_mul_f32 v55, v53, v42
	s_nop 0
	v_max_f32 v55, v53, v55
	v_mul_f32 v53, v54, v42
	s_nop 0
	v_max_f32 v59, v54, v53
	v_mul_f32 v53, v56, v57
	s_nop 0
	v_mul_f32 v54, v53, v42
	s_nop 0
	v_max_f32 v60, v53, v54
	v_mul_f32 v53, v2, v42
	s_nop 0
	v_max_f32 v2, v2, v53
	v_mul_f32 v53, v3, v3
	s_nop 0
	v_fma_f32 v53, v4, v4, v53
	s_nop 0
	v_fma_f32 v53, v52, v52, v53
	s_nop 0
	v_fma_f32 v53, v58, v58, v53
	s_nop 0
	v_fma_f32 v53, v55, v55, v53
	s_nop 0
	v_fma_f32 v53, v59, v59, v53
	s_nop 0
	v_fma_f32 v53, v60, v60, v53
	s_nop 0
	v_fma_f32 v53, v2, v2, v53
	s_nop 1
	v_add_f32_dpp v53, v53, v53 quad_perm:[1,0,3,2] row_mask:0xf bank_mask:0xf bound_ctrl:1
	s_nop 1
	v_add_f32_dpp v53, v53, v53 quad_perm:[2,3,0,1] row_mask:0xf bank_mask:0xf bound_ctrl:1
	s_waitcnt lgkmcnt(0)
	s_nop 1
	v_add_f32_dpp v53, v53, v53 row_half_mirror row_mask:0xf bank_mask:0xf bound_ctrl:1
	s_nop 1
	v_add_f32_dpp v53, v53, v53 row_ror:8 row_mask:0xf bank_mask:0xf bound_ctrl:1
	v_mov_b32_e32 v54, v53
	s_nop 1
	v_permlane16_swap_b32 v54, v53
	s_waitcnt lgkmcnt(0)
	v_add_f32_e32 v53, v53, v54
	v_mov_b32_e32 v54, v53
	s_nop 1
	v_permlane32_swap_b32 v54, v53
	s_waitcnt lgkmcnt(0)
	v_add_f32_e32 v53, v53, v54
	v_mul_f32_e32 v54, 0x4f800000, v53
	v_cmp_gt_f32_e32 vcc, s17, v53
	s_nop 1
	v_cndmask_b32_e32 v53, v53, v54, vcc
	v_sqrt_f32_e32 v54, v53
	s_nop 0
	v_add_u32_e32 v56, -1, v54
	v_fma_f32 v57, -v56, v54, v53
	v_cmp_ge_f32_e64 s[8:9], 0, v57
	v_add_u32_e32 v57, 1, v54
	s_nop 0
	v_cndmask_b32_e64 v56, v54, v56, s[8:9]
	v_fma_f32 v54, -v57, v54, v53
	v_cmp_lt_f32_e64 s[8:9], 0, v54
	s_nop 1
	v_cndmask_b32_e64 v54, v56, v57, s[8:9]
	v_mul_f32_e32 v56, 0x37800000, v54
	v_cndmask_b32_e32 v54, v54, v56, vcc
	v_cmp_class_f32_e32 vcc, v53, v41
	s_nop 1
	v_cndmask_b32_e32 v53, v54, v53, vcc
	v_div_scale_f32 v54, s[8:9], v53, v53, 1.0
	v_rcp_f32_e32 v56, v54
	s_nop 0
	v_fma_f32 v57, -v54, v56, 1.0
	v_fmac_f32_e32 v56, v57, v56
	v_div_scale_f32 v57, vcc, 1.0, v53, 1.0
	v_mul_f32_e32 v61, v57, v56
	v_fma_f32 v62, -v54, v61, v57
	v_fmac_f32_e32 v61, v62, v56
	v_fma_f32 v54, -v54, v61, v57
	v_div_fmas_f32 v54, v54, v56, v61
	v_div_fixup_f32 v61, v54, v53, 1.0
	v_mul_f32 v54, v3, v61
	v_mul_f32 v3, v4, v61
	v_mul_f32 v53, v52, v61
	v_mul_f32 v57, v58, v61
	v_mul_f32 v52, v55, v61
	v_mul_f32 v56, v59, v61
	v_mul_f32 v55, v60, v61
	v_mul_f32 v58, v2, v61
	s_branch .LBB0_11
